# mixer-phase work queue order: three conversion chunks per mixer unit while chunks last
# baseline (speedup 1.0000x reference)
.LBB0_893:
	s_or_b64 exec, exec, s[36:37]
	v_readlane_b32 s2, v255, 15
	s_waitcnt lgkmcnt(0)
	s_barrier
	v_mov_b32_e32 v0, s2
	ds_read_b32 v0, v0
	s_and_b64 s[2:3], s[70:71], exec
	s_movk_i32 s2, 0x3a8
	s_cselect_b32 s27, s2, 0x270
	s_or_b32 s97, s27, 0x400
	s_waitcnt lgkmcnt(0)
	v_cmp_le_u32_e32 vcc, s97, v0
	v_readfirstlane_b32 s7, v0
	s_cbranch_vccnz .LBB0_1552
	s_add_u32 s72, s20, 0x40200000
	s_addc_u32 s73, s21, 0
	s_add_u32 s80, s20, 0x53800000
	v_writelane_b32 v255, s78, 40
	s_addc_u32 s81, s21, 0
	s_add_u32 s2, s20, 0x53600000
	v_writelane_b32 v255, s79, 41
	v_writelane_b32 v255, s2, 42
	s_addc_u32 s2, s21, 0
	v_writelane_b32 v255, s2, 43
	v_writelane_b32 v255, s70, 44
	s_and_b64 s[2:3], s[70:71], exec
	s_movk_i32 s2, 0x4e00
	v_writelane_b32 v255, s71, 45
	s_cselect_b32 s78, s2, 0x13800
	v_readlane_b32 s2, v255, 36
	v_readlane_b32 s3, v255, 37
	s_mul_hi_u32 s79, s27, 0xaaaaaaab
	s_lshr_b32 s79, s79, 1
	s_add_i32 s79, s79, s27
	s_lshl_b32 s3, s2, 4
	s_lshl_b32 s2, s2, 3
	s_add_u32 s71, s20, 0x24200000
	v_writelane_b32 v255, s3, 46
	s_addc_u32 s23, s21, 0
	v_writelane_b32 v255, s2, 47
	s_add_u32 s2, s20, 0x90000
	v_writelane_b32 v255, s2, 48
	s_addc_u32 s2, s21, 0
	s_add_u32 s70, s20, 0x14200000
	v_writelane_b32 v255, s2, 49
	s_addc_u32 s2, s21, 0
	s_add_u32 s16, s20, 0x10200000
	s_addc_u32 s3, s21, 0
	s_add_u32 s74, s20, 0xd200000
	s_addc_u32 s75, s21, 0
	s_add_u32 s30, s20, 0x110000
	s_addc_u32 s31, s21, 0
	s_add_u32 s17, s20, 0x200000
	s_addc_u32 s12, s21, 0
	s_add_u32 s13, s20, 0x137000
	s_addc_u32 s5, s21, 0
	s_add_u32 s34, s20, 0x2a00000
	v_readlane_b32 s8, v255, 11
	s_addc_u32 s35, s21, 0
	s_add_i32 s8, s78, s8
	v_writelane_b32 v255, s8, 50
	s_add_i32 s83, s78, 0xffffb200
	v_readlane_b32 s8, v255, 9
	s_add_i32 s8, s8, s78
	v_mov_b32_e32 v213, 0
	v_writelane_b32 v255, s8, 51
	s_nop 0
	v_readlane_b32 s8, v255, 10
	s_add_i32 s8, s8, s78
	s_nop 0
	v_writelane_b32 v255, s8, 52
	s_nop 0
	v_readlane_b32 s8, v255, 12
	s_add_i32 s8, s8, s78
	s_nop 0
	v_writelane_b32 v255, s8, 53
	s_branch .LBB0_896

.LBB0_917:
	s_lshr_b32 s8, s7, 2
	s_mul_i32 s10, s8, 4
	s_sub_i32 s10, s7, s10
	s_mul_i32 s7, s8, 3
	s_add_i32 s7, s7, s10
	s_add_i32 s7, s7, -1
	s_cmp_eq_u32 s10, 0
	s_cselect_b32 s26, -1, s7
	s_cselect_b32 s28, s8, -1
	s_cmp_lt_i32 s26, 0
	s_mov_b64 s[38:39], -1
	s_cbranch_scc1 .LBB0_903
